# GEMM1: next-tile row-list load no longer drained at the unit top (row-table write deferred into the first trip)
# baseline (speedup 1.0000x reference)
.LBB0_904:
	s_mov_b32 s98, 0
	s_cmp_lg_u32 s48, s71
	s_cselect_b64 s[38:39], -1, 0
	s_and_b64 s[38:39], s[34:35], s[38:39]
	s_andn2_b64 vcc, exec, s[38:39]
	s_cbranch_vccnz .LBB0_910
	v_mbcnt_lo_u32_b32 v128, -1, 0
	v_mbcnt_hi_u32_b32 v128, -1, v128
	s_xor_b32 s55, s55, 1
	s_mov_b32 s98, 1
	v_mov_b32_e32 v229, 0
	v_add_u32_e32 v130, s33, v128
	v_cmp_gt_i32_e32 vcc, s64, v130
	s_and_saveexec_b64 s[38:39], vcc
	s_cbranch_execz .LBB0_909
	s_lshl_b32 s7, s26, 2
	v_readlane_b32 s42, v254, 13
	s_add_i32 s7, s7, 0x248a0
	v_readlane_b32 s43, v254, 14
	v_mov_b32_e32 v128, s7
	ds_read_b32 v129, v128
	v_lshl_add_u32 v128, s72, 8, v130
	s_waitcnt lgkmcnt(0)
	v_cmp_lt_i32_e32 vcc, v128, v129
	v_mov_b32_e32 v129, 0
	s_and_saveexec_b64 s[40:41], vcc
	s_cbranch_execz .LBB0_908
	s_mov_b64 s[42:43], s[100:101]
	s_ashr_i32 s27, s26, 31
	s_lshl_b64 s[76:77], s[26:27], 17
	v_ashrrev_i32_e32 v129, 31, v128
	s_waitcnt lgkmcnt(0)
	s_add_u32 s42, s42, s76
	s_addc_u32 s43, s43, s77
	v_lshl_add_u64 v[128:129], v[128:129], 2, s[42:43]
	v_add_co_u32_e32 v128, vcc, 0x1a00000, v128
	s_nop 1
	v_addc_co_u32_e32 v129, vcc, 0, v129, vcc
	global_load_dword v229, v[128:129], off
.LBB0_908:
	s_or_b64 exec, exec, s[40:41]
.LBB0_909:
	s_or_b64 exec, exec, s[38:39]
.LBB0_910:
	s_add_u32 s25, s36, 0x100
	s_addc_u32 s27, s37, 0
	s_lshl_b32 s7, s55, 10
	s_add_i32 s7, s7, 0x24000
	s_mov_b32 s42, -2
	s_mov_b64 s[36:37], 0
	s_cmp_eq_u32 s42, 12
	s_cselect_b64 s[40:41], -1, 0
	s_and_b64 s[38:39], s[34:35], s[40:41]
	s_andn2_b64 vcc, exec, s[38:39]
	v_mov_b32_e32 v128, v186
	v_mov_b32_e32 v129, v176
	s_add_u32 s76, s10, s36
	v_add_u32_e32 v134, s67, v194
	v_add_u32_e32 v142, s67, v195
	v_add_u32_e32 v150, s68, v194
	v_add_u32_e32 v158, s68, v195
	s_addc_u32 s77, s11, s37
	ds_read_b128 v[130:133], v134
	ds_read_b128 v[138:141], v134 offset:2048
	ds_read_b128 v[134:137], v142
	ds_read_b128 v[142:145], v142 offset:2048
	ds_read_b128 v[146:149], v150
	ds_read_b128 v[154:157], v150 offset:2048
	ds_read_b128 v[150:153], v158
	ds_read_b128 v[158:161], v158 offset:2048
	s_add_u32 s43, s76, 0x36000100
	s_addc_u32 s75, s77, 0
	s_and_b64 s[38:39], s[40:41], exec
	s_cselect_b32 s39, s13, s75
	s_cselect_b32 s38, s12, s43
	s_add_u32 s43, s25, s36
	s_addc_u32 s75, s27, s37
	s_and_b64 s[40:41], s[40:41], exec
	s_cselect_b32 s41, s31, s75
	s_cselect_b32 s40, s30, s43
	ds_read_b128 v[162:165], v227
	ds_read_b128 v[232:235], v227 offset:2048
	ds_read_b128 v[166:169], v228
	ds_read_b128 v[236:239], v228 offset:2048
	ds_read_b128 v[240:243], v227 offset:4096
	ds_read_b128 v[196:199], v227 offset:6144
	ds_read_b128 v[244:247], v228 offset:4096
	ds_read_b128 v[200:203], v228 offset:6144
	s_add_i32 m0, s50, 0xc000
	v_lshl_add_u64 v[170:171], s[76:77], 0, v[176:177]
	v_lshl_add_u64 v[170:171], v[170:171], 0, s[16:17]
	v_mov_b32_e32 v187, v177
	global_load_lds_dwordx4 v[170:171], off
	s_add_i32 m0, s50, 0xe000
	v_lshl_add_u64 v[170:171], s[76:77], 0, v[186:187]
	v_lshl_add_u64 v[170:171], v[170:171], 0, s[16:17]
	global_load_lds_dwordx4 v[170:171], off
	s_waitcnt vmcnt(8)
	s_waitcnt lgkmcnt(0)
	s_barrier
	s_setprio 1
	s_waitcnt lgkmcnt(0)
	v_mfma_f32_16x16x128_f8f6f4 v[100:103], v[130:137], v[162:169], 0
	v_mfma_f32_16x16x128_f8f6f4 v[96:99], v[138:145], v[162:169], 0
	v_mfma_f32_16x16x128_f8f6f4 v[92:95], v[130:137], v[232:239], 0
	v_mfma_f32_16x16x128_f8f6f4 v[88:91], v[138:145], v[232:239], 0
	v_mfma_f32_16x16x128_f8f6f4 v[84:87], v[130:137], v[240:247], 0
	v_mfma_f32_16x16x128_f8f6f4 v[80:83], v[138:145], v[240:247], 0
	v_mfma_f32_16x16x128_f8f6f4 v[170:173], v[130:137], v[196:203], 0
	v_mfma_f32_16x16x128_f8f6f4 v[188:191], v[138:145], v[196:203], 0
	s_setprio 0
	s_setprio 1
	v_mfma_f32_16x16x128_f8f6f4 v[40:43], v[146:153], v[196:203], 0
	v_mfma_f32_16x16x128_f8f6f4 v[32:35], v[154:161], v[196:203], 0
	v_mfma_f32_16x16x128_f8f6f4 v[248:251], v[146:153], v[162:169], 0
	v_mfma_f32_16x16x128_f8f6f4 v[204:207], v[154:161], v[162:169], 0
	v_mfma_f32_16x16x128_f8f6f4 v[208:211], v[146:153], v[232:239], 0
	v_mfma_f32_16x16x128_f8f6f4 v[212:215], v[154:161], v[232:239], 0
	v_mfma_f32_16x16x128_f8f6f4 v[216:219], v[146:153], v[240:247], 0
	v_mfma_f32_16x16x128_f8f6f4 v[240:243], v[154:161], v[240:247], 0
	s_setprio 0
	s_barrier
	s_add_i32 s43, s67, s5
	s_mov_b32 m0, s43
	s_nop 2
	ds_read_b128 v[48:51], v227 offset:16384
	ds_read_b128 v[56:59], v227 offset:18432
	ds_read_b128 v[52:55], v228 offset:16384
	ds_read_b128 v[60:63], v228 offset:18432
	ds_read_b128 v[64:67], v227 offset:20480
	ds_read_b128 v[72:75], v227 offset:22528
	ds_read_b128 v[68:71], v228 offset:20480
	ds_read_b128 v[76:79], v228 offset:22528
	s_nop 0
	global_load_lds_dwordx4 v184, s[40:41]
	s_add_i32 m0, s43, 0x2000
	s_add_u32 s76, s40, 0x4000
	s_addc_u32 s77, s41, 0
	s_add_i32 s43, s68, s5
	s_nop 0
	global_load_lds_dwordx4 v178, s[40:41]
	s_mov_b32 m0, s43
	s_nop 0
	global_load_lds_dwordx4 v184, s[76:77]
	s_add_i32 m0, s43, 0x2000
	s_nop 0
	global_load_lds_dwordx4 v178, s[76:77]
	s_waitcnt vmcnt(6)
	s_cmp_eq_u32 s98, 0
	s_cbranch_scc1 .Lprep6_done
	s_cmpk_ge_u32 s33, 0x100
	s_cbranch_scc1 .Lprep6_done
	v_mbcnt_lo_u32_b32 v220, -1, 0
	v_mbcnt_hi_u32_b32 v220, -1, v220
	v_add_u32_e32 v220, s33, v220
	v_lshlrev_b32_e32 v220, 2, v220
	v_lshl_add_u32 v220, s55, 10, v220
	v_add_u32_e32 v220, 0x24000, v220
	v_lshlrev_b32_e32 v229, 9, v229
	v_and_b32_e32 v229, 0xfffff800, v229
	ds_write_b32 v220, v229
.Lprep6_done:
	s_waitcnt lgkmcnt(0)
	s_barrier
	s_setprio 1
	s_waitcnt lgkmcnt(0)
	v_mfma_f32_16x16x128_f8f6f4 v[44:47], v[130:137], v[48:55], 0
	v_mfma_f32_16x16x128_f8f6f4 v[36:39], v[138:145], v[48:55], 0
	v_mfma_f32_16x16x128_f8f6f4 v[28:31], v[130:137], v[56:63], 0
	v_mfma_f32_16x16x128_f8f6f4 v[24:27], v[138:145], v[56:63], 0
	v_mfma_f32_16x16x128_f8f6f4 v[20:23], v[130:137], v[64:71], 0
	v_mfma_f32_16x16x128_f8f6f4 v[16:19], v[138:145], v[64:71], 0
	v_mfma_f32_16x16x128_f8f6f4 v[12:15], v[130:137], v[72:79], 0
	v_mfma_f32_16x16x128_f8f6f4 v[8:11], v[138:145], v[72:79], 0
	s_setprio 0
	s_setprio 1
	v_mfma_f32_16x16x128_f8f6f4 v[4:7], v[146:153], v[48:55], 0
	v_mfma_f32_16x16x128_f8f6f4 v[0:3], v[154:161], v[48:55], 0
	v_mfma_f32_16x16x128_f8f6f4 v[104:107], v[146:153], v[56:63], 0
	v_mfma_f32_16x16x128_f8f6f4 v[108:111], v[154:161], v[56:63], 0
	v_mfma_f32_16x16x128_f8f6f4 v[112:115], v[146:153], v[64:71], 0
	v_mfma_f32_16x16x128_f8f6f4 v[116:119], v[154:161], v[64:71], 0
	v_mfma_f32_16x16x128_f8f6f4 v[120:123], v[146:153], v[72:79], 0
	v_mfma_f32_16x16x128_f8f6f4 v[124:127], v[154:161], v[72:79], 0
	s_setprio 0
	s_barrier
	s_add_i32 s43, 0, 0x18000
	v_add_u32_e32 v48, s43, v194
	s_add_i32 s75, 0, 0x1c000
	v_add_u32_e32 v49, s43, v195
	ds_read_b128 v[130:133], v48
	ds_read_b128 v[138:141], v48 offset:2048
	ds_read_b128 v[134:137], v49
	ds_read_b128 v[142:145], v49 offset:2048
	v_add_u32_e32 v48, s75, v194
	v_add_u32_e32 v49, s75, v195
	ds_read_b128 v[146:149], v48
	ds_read_b128 v[154:157], v48 offset:2048
	ds_read_b128 v[150:153], v49
	ds_read_b128 v[158:161], v49 offset:2048
	s_mov_b32 m0, s52
	v_mov_b32_e32 v176, v129
	ds_read_b128 v[48:51], v227 offset:32768
	ds_read_b128 v[162:165], v227 offset:34816
	ds_read_b128 v[52:55], v228 offset:32768
	ds_read_b128 v[166:169], v228 offset:34816
	ds_read_b128 v[196:199], v227 offset:36864
	ds_read_b128 v[232:235], v227 offset:38912
	ds_read_b128 v[200:203], v228 offset:36864
	ds_read_b128 v[236:239], v228 offset:38912
	s_mov_b32 m0, s50
	s_nop 0
	global_load_lds_dwordx4 v180, s[38:39]
	s_mov_b32 m0, s51
	s_nop 0
	global_load_lds_dwordx4 v182, s[38:39]
	s_mov_b32 m0, s52
	v_mov_b32_e32 v186, v128
	global_load_lds_dwordx4 v176, s[38:39]
	s_mov_b32 m0, s53
	s_nop 0
	global_load_lds_dwordx4 v186, s[38:39]
	s_waitcnt vmcnt(8)
	s_waitcnt lgkmcnt(0)
	s_barrier
	s_setprio 1
	s_waitcnt lgkmcnt(0)
	v_mfma_f32_16x16x128_f8f6f4 v[100:103], v[130:137], v[48:55], v[100:103]
	v_mfma_f32_16x16x128_f8f6f4 v[96:99], v[138:145], v[48:55], v[96:99]
	v_mfma_f32_16x16x128_f8f6f4 v[92:95], v[130:137], v[162:169], v[92:95]
	v_mfma_f32_16x16x128_f8f6f4 v[88:91], v[138:145], v[162:169], v[88:91]
	v_mfma_f32_16x16x128_f8f6f4 v[84:87], v[130:137], v[196:203], v[84:87]
	v_mfma_f32_16x16x128_f8f6f4 v[80:83], v[138:145], v[196:203], v[80:83]
	v_mfma_f32_16x16x128_f8f6f4 v[76:79], v[130:137], v[232:239], v[170:173]
	v_mfma_f32_16x16x128_f8f6f4 v[72:75], v[138:145], v[232:239], v[188:191]
	s_setprio 0
	s_setprio 1
	v_mfma_f32_16x16x128_f8f6f4 v[68:71], v[146:153], v[48:55], v[248:251]
	v_mfma_f32_16x16x128_f8f6f4 v[64:67], v[154:161], v[48:55], v[204:207]
	v_mfma_f32_16x16x128_f8f6f4 v[60:63], v[146:153], v[162:169], v[208:211]
	v_mfma_f32_16x16x128_f8f6f4 v[56:59], v[154:161], v[162:169], v[212:215]
	v_mfma_f32_16x16x128_f8f6f4 v[52:55], v[146:153], v[196:203], v[216:219]
	v_mfma_f32_16x16x128_f8f6f4 v[48:51], v[154:161], v[196:203], v[240:243]
	v_mfma_f32_16x16x128_f8f6f4 v[40:43], v[146:153], v[232:239], v[40:43]
	v_mfma_f32_16x16x128_f8f6f4 v[32:35], v[154:161], v[232:239], v[32:35]
	s_setprio 0
	s_barrier
	v_mov_b32_e32 v185, v177
	ds_read_b128 v[162:165], v227 offset:49152
	ds_read_b128 v[196:199], v227 offset:51200
	ds_read_b128 v[166:169], v228 offset:49152
	ds_read_b128 v[200:203], v228 offset:51200
	ds_read_b128 v[232:235], v227 offset:53248
	ds_read_b128 v[240:243], v227 offset:55296
	ds_read_b128 v[236:239], v228 offset:53248
	ds_read_b128 v[244:247], v228 offset:55296
	s_add_i32 s43, s43, s5
	v_lshl_add_u64 v[128:129], s[40:41], 0, v[184:185]
	v_lshl_add_u64 v[128:129], v[128:129], 0, s[14:15]
	s_mov_b32 m0, s43
	v_mov_b32_e32 v179, v177
	global_load_lds_dwordx4 v[128:129], off
	s_add_i32 m0, s43, 0x2000
	v_mov_b32_e32 v181, v177
	v_lshl_add_u64 v[128:129], s[40:41], 0, v[178:179]
	s_add_u32 s40, s40, 0x4080
	v_lshl_add_u64 v[128:129], v[128:129], 0, s[14:15]
	s_addc_u32 s41, s41, 0
	s_add_i32 s43, s75, s5
	global_load_lds_dwordx4 v[128:129], off
	s_mov_b32 m0, s43
	v_mov_b32_e32 v183, v177
	global_load_lds_dwordx4 v184, s[40:41]
	s_add_i32 m0, s43, 0x2000
	s_nop 0
	global_load_lds_dwordx4 v178, s[40:41]
	s_mov_b32 m0, s62
	v_lshl_add_u64 v[128:129], s[38:39], 0, v[180:181]
	v_lshl_add_u64 v[128:129], v[128:129], 0, s[14:15]
	global_load_lds_dwordx4 v[128:129], off
	s_mov_b32 m0, s63
	v_lshl_add_u64 v[128:129], s[38:39], 0, v[182:183]
	v_lshl_add_u64 v[128:129], v[128:129], 0, s[14:15]
	global_load_lds_dwordx4 v[128:129], off
	s_waitcnt vmcnt(8)
	s_waitcnt lgkmcnt(0)
	s_barrier
	s_setprio 1
	s_waitcnt lgkmcnt(0)
	v_mfma_f32_16x16x128_f8f6f4 v[44:47], v[130:137], v[162:169], v[44:47]
	v_mfma_f32_16x16x128_f8f6f4 v[36:39], v[138:145], v[162:169], v[36:39]
	v_mfma_f32_16x16x128_f8f6f4 v[28:31], v[130:137], v[196:203], v[28:31]
	v_mfma_f32_16x16x128_f8f6f4 v[24:27], v[138:145], v[196:203], v[24:27]
	v_mfma_f32_16x16x128_f8f6f4 v[20:23], v[130:137], v[232:239], v[20:23]
	v_mfma_f32_16x16x128_f8f6f4 v[16:19], v[138:145], v[232:239], v[16:19]
	v_mfma_f32_16x16x128_f8f6f4 v[12:15], v[130:137], v[240:247], v[12:15]
	v_mfma_f32_16x16x128_f8f6f4 v[8:11], v[138:145], v[240:247], v[8:11]
	s_setprio 0
	s_setprio 1
	v_mfma_f32_16x16x128_f8f6f4 v[4:7], v[146:153], v[162:169], v[4:7]
	v_mfma_f32_16x16x128_f8f6f4 v[0:3], v[154:161], v[162:169], v[0:3]
	v_mfma_f32_16x16x128_f8f6f4 v[104:107], v[146:153], v[196:203], v[104:107]
	v_mfma_f32_16x16x128_f8f6f4 v[108:111], v[154:161], v[196:203], v[108:111]
	v_mfma_f32_16x16x128_f8f6f4 v[112:115], v[146:153], v[232:239], v[112:115]
	v_mfma_f32_16x16x128_f8f6f4 v[116:119], v[154:161], v[232:239], v[116:119]
	v_mfma_f32_16x16x128_f8f6f4 v[120:123], v[146:153], v[240:247], v[120:123]
	v_mfma_f32_16x16x128_f8f6f4 v[124:127], v[154:161], v[240:247], v[124:127]
	s_setprio 0
	s_barrier
	s_add_i32 s42, s42, 2
	s_add_u32 s36, s36, 0x100
	s_addc_u32 s37, s37, 0
	s_branch .LBB0_912
